# v41 + S3 fwd head-norm reduction via permlane swaps (no rdec move)
# speedup vs baseline: 1.0003x; 1.0003x over previous
.LBB0_714:
	v_add_u32_e32 v18, 1, v121
	v_cvt_f32_ubyte0_e32 v18, v18
	v_mul_f32_e32 v18, v64, v18
	v_mul_f32_e32 v18, 0xbfb8aa3b, v18
	v_add_u32_e32 v10, s91, v10
	v_exp_f32_e32 v54, v18
	v_cvt_pk_bf16_f32 v18, v14, v13
	v_lshlrev_b32_e32 v13, 4, v10
	v_and_b32_e32 v13, 0xfffffc00, v13
	v_bitop3_b32 v10, v10, v11, 56 bitop3:0x6c
	v_add3_u32 v10, v15, v13, v10
	v_cvt_pk_bf16_f32 v19, v16, v17
	ds_write_b64 v10, v[18:19]
	s_waitcnt lgkmcnt(0)
	s_barrier
	v_add_u32_e32 v55, s97, v12
	v_add_u32_e32 v123, s3, v12
	v_add_u32_e32 v194, s62, v12
	ds_read_b128 v[14:17], v9
	ds_read_b128 v[18:21], v55
	ds_read_b128 v[22:25], v55 offset:4096
	ds_read_b128 v[26:29], v55 offset:8192
	ds_read_b128 v[30:33], v55 offset:12288
	v_add_u32_e32 v195, s61, v12
	ds_read_b128 v[10:13], v9 offset:1024
	ds_read_b128 v[34:37], v55 offset:1024
	ds_read_b128 v[38:41], v55 offset:5120
	ds_read_b128 v[42:45], v55 offset:9216
	ds_read_b128 v[46:49], v55 offset:13312
	ds_read_b128 v[50:53], v9 offset:2048
	ds_read_b128 v[124:127], v55 offset:2048
	ds_read_b128 v[128:131], v55 offset:6144
	ds_read_b128 v[132:135], v55 offset:10240
	ds_read_b128 v[136:139], v55 offset:14336
	s_waitcnt lgkmcnt(13)
	v_mfma_f32_16x16x32_bf16 v[18:21], v[18:21], v[14:17], 0
	s_waitcnt lgkmcnt(12)
	v_mfma_f32_16x16x32_bf16 v[22:25], v[22:25], v[14:17], 0
	s_waitcnt lgkmcnt(11)
	v_mfma_f32_16x16x32_bf16 v[26:29], v[26:29], v[14:17], 0
	s_waitcnt lgkmcnt(10)
	v_mfma_f32_16x16x32_bf16 v[14:17], v[30:33], v[14:17], 0
	s_waitcnt lgkmcnt(8)
	v_mfma_f32_16x16x32_bf16 v[18:21], v[34:37], v[10:13], v[18:21]
	ds_read_b128 v[30:33], v9 offset:3072
	s_waitcnt lgkmcnt(8)
	v_mfma_f32_16x16x32_bf16 v[22:25], v[38:41], v[10:13], v[22:25]
	s_waitcnt lgkmcnt(7)
	v_mfma_f32_16x16x32_bf16 v[26:29], v[42:45], v[10:13], v[26:29]
	ds_read_b128 v[34:37], v55 offset:3072
	ds_read_b128 v[38:41], v55 offset:7168
	ds_read_b128 v[42:45], v55 offset:11264
	ds_read_b128 v[212:215], v55 offset:15360
	s_waitcnt lgkmcnt(10)
	v_mfma_f32_16x16x32_bf16 v[10:13], v[46:49], v[10:13], v[14:17]
	s_waitcnt lgkmcnt(8)
	v_mfma_f32_16x16x32_bf16 v[14:17], v[124:127], v[50:53], v[18:21]
	s_waitcnt lgkmcnt(7)
	v_mfma_f32_16x16x32_bf16 v[18:21], v[128:131], v[50:53], v[22:25]
	s_nop 2
	ds_read_b128 v[22:25], v123
	ds_read_b128 v[46:49], v195 offset:49152
	s_waitcnt lgkmcnt(8)
	v_mfma_f32_16x16x32_bf16 v[26:29], v[132:135], v[50:53], v[26:29]
	ds_read_b128 v[124:127], v195 offset:51200
	ds_read_b128 v[128:131], v195 offset:53248
	ds_read_b128 v[132:135], v195 offset:55296
	s_waitcnt lgkmcnt(10)
	v_mfma_f32_16x16x32_bf16 v[10:13], v[136:139], v[50:53], v[10:13]
	s_waitcnt lgkmcnt(8)
	v_mfma_f32_16x16x32_bf16 v[14:17], v[34:37], v[30:33], v[14:17]
	s_waitcnt lgkmcnt(7)
	v_mfma_f32_16x16x32_bf16 v[18:21], v[38:41], v[30:33], v[18:21]
	ds_read_b128 v[34:37], v123 offset:1024
	ds_read_b128 v[38:41], v195 offset:50176
	s_waitcnt lgkmcnt(8)
	v_mfma_f32_16x16x32_bf16 v[26:29], v[42:45], v[30:33], v[26:29]
	ds_read_b128 v[42:45], v195 offset:52224
	ds_read_b128 v[136:139], v195 offset:54272
	ds_read_b128 v[216:219], v195 offset:56320
	s_waitcnt lgkmcnt(10)
	v_mfma_f32_16x16x32_bf16 v[10:13], v[212:215], v[30:33], v[10:13]
	v_mul_f32_e64 v20, v54, v20
	v_mul_f32_e64 v21, v54, v21
	v_pk_mul_f32 v[18:19], v[54:55], v[18:19] op_sel_hi:[0,1]
	v_pk_mul_f32 v[28:29], v[54:55], v[28:29] op_sel_hi:[0,1]
	v_pk_mul_f32 v[26:27], v[54:55], v[26:27] op_sel_hi:[0,1]
	s_waitcnt lgkmcnt(7)
	v_mfma_f32_16x16x32_bf16 v[18:21], v[124:127], v[22:25], v[18:21]
	ds_read_b128 v[124:127], v194 offset:32768
	ds_read_b128 v[212:215], v194 offset:33792
	v_pk_mul_f32 v[16:17], v[54:55], v[16:17] op_sel_hi:[0,1]
	v_pk_mul_f32 v[14:15], v[54:55], v[14:15] op_sel_hi:[0,1]
	s_waitcnt lgkmcnt(8)
	v_mfma_f32_16x16x32_bf16 v[26:29], v[128:131], v[22:25], v[26:29]
	ds_read_b128 v[30:33], v8 offset:49152
	ds_read_b128 v[128:131], v8 offset:50176
	ds_read_b128 v[220:223], v8 offset:51200
	ds_read_b128 v[224:227], v8 offset:52224
	v_pk_mul_f32 v[12:13], v[54:55], v[12:13] op_sel_hi:[0,1]
	v_pk_mul_f32 v[10:11], v[54:55], v[10:11] op_sel_hi:[0,1]
	v_mfma_f32_16x16x32_bf16 v[14:17], v[46:49], v[22:25], v[14:17]
	s_waitcnt lgkmcnt(11)
	v_mfma_f32_16x16x32_bf16 v[10:13], v[132:135], v[22:25], v[10:13]
	s_waitcnt lgkmcnt(9)
	v_mfma_f32_16x16x32_bf16 v[52:55], v[38:41], v[34:37], v[14:17]
	s_waitcnt lgkmcnt(8)
	v_mfma_f32_16x16x32_bf16 v[48:51], v[42:45], v[34:37], v[18:21]
	s_waitcnt lgkmcnt(7)
	v_mfma_f32_16x16x32_bf16 v[40:43], v[136:139], v[34:37], v[26:29]
	ds_read_b128 v[14:17], v8 offset:53248
	ds_read_b128 v[18:21], v8 offset:54272
	ds_read_b128 v[132:135], v8 offset:55296
	ds_read_b128 v[136:139], v8 offset:56320
	s_waitcnt lgkmcnt(10)
	v_mfma_f32_16x16x32_bf16 v[44:47], v[216:219], v[34:37], v[10:13]
	s_waitcnt lgkmcnt(7)
	v_mfma_f32_16x16x32_bf16 v[10:13], v[124:127], v[30:33], 0
	s_waitcnt lgkmcnt(6)
	v_mfma_f32_16x16x32_bf16 v[36:39], v[212:215], v[128:131], v[10:13]
	s_waitcnt lgkmcnt(5)
	v_mfma_f32_16x16x32_bf16 v[10:13], v[124:127], v[220:223], 0
	s_waitcnt lgkmcnt(4)
	v_mfma_f32_16x16x32_bf16 v[32:35], v[212:215], v[224:227], v[10:13]
	s_waitcnt lgkmcnt(3)
	v_mfma_f32_16x16x32_bf16 v[10:13], v[124:127], v[14:17], 0
	s_waitcnt lgkmcnt(2)
	v_mfma_f32_16x16x32_bf16 v[24:27], v[212:215], v[18:21], v[10:13]
	s_nop 5
	ds_read_b128 v[10:13], v8 offset:57344
	ds_read_b128 v[14:17], v8 offset:58368
	ds_read_b128 v[128:131], v8 offset:59392
	ds_read_b128 v[216:219], v8 offset:60416
	s_waitcnt lgkmcnt(5)
	v_mfma_f32_16x16x32_bf16 v[18:21], v[124:127], v[132:135], 0
	ds_read_b128 v[132:135], v8 offset:61440
	ds_read_b128 v[220:223], v8 offset:62464
	ds_read_b128 v[224:227], v8 offset:63488
	ds_read_b128 v[228:231], v8 offset:64512
	s_waitcnt lgkmcnt(8)
	v_mfma_f32_16x16x32_bf16 v[28:31], v[212:215], v[136:139], v[18:21]
	s_waitcnt lgkmcnt(7)
	v_mfma_f32_16x16x32_bf16 v[8:11], v[124:127], v[10:13], 0
	s_mov_b64 s[56:57], -1
	s_andn2_b64 vcc, exec, s[54:55]
	s_waitcnt lgkmcnt(6)
	v_mfma_f32_16x16x32_bf16 v[20:23], v[212:215], v[14:17], v[8:11]
	s_waitcnt lgkmcnt(5)
	v_mfma_f32_16x16x32_bf16 v[8:11], v[124:127], v[128:131], 0
	s_waitcnt lgkmcnt(4)
	v_mfma_f32_16x16x32_bf16 v[16:19], v[212:215], v[216:219], v[8:11]
	s_waitcnt lgkmcnt(3)
	v_mfma_f32_16x16x32_bf16 v[8:11], v[124:127], v[132:135], 0
	s_waitcnt lgkmcnt(2)
	v_mfma_f32_16x16x32_bf16 v[12:15], v[212:215], v[220:223], v[8:11]
	s_waitcnt lgkmcnt(1)
	v_mfma_f32_16x16x32_bf16 v[8:11], v[124:127], v[224:227], 0
	s_waitcnt lgkmcnt(0)
	v_mfma_f32_16x16x32_bf16 v[8:11], v[212:215], v[228:231], v[8:11]
	s_cbranch_vccnz .LBB0_718
	s_waitcnt vmcnt(1)
	v_lshlrev_b32_e32 v124, 16, v0
	v_and_b32_e32 v125, 0xffff0000, v0
	v_lshlrev_b32_e32 v126, 16, v1
	v_and_b32_e32 v127, 0xffff0000, v1
	v_pk_add_f32 v[136:137], v[54:55], v[126:127]
	v_pk_add_f32 v[138:139], v[52:53], v[124:125]
	v_mul_f32_e32 v124, v137, v137
	v_mul_f32_e32 v123, v139, v139
	v_fmac_f32_e32 v123, v138, v138
	v_fmac_f32_e32 v124, v136, v136
	v_add_f32_e32 v123, v123, v124
	v_lshlrev_b32_e32 v124, 16, v2
	v_and_b32_e32 v125, 0xffff0000, v2
	v_lshlrev_b32_e32 v126, 16, v3
	v_and_b32_e32 v127, 0xffff0000, v3
	v_pk_add_f32 v[132:133], v[50:51], v[126:127]
	v_pk_add_f32 v[134:135], v[48:49], v[124:125]
	v_mul_f32_e32 v125, v133, v133
	v_mul_f32_e32 v124, v135, v135
	v_fmac_f32_e32 v124, v134, v134
	v_fmac_f32_e32 v125, v132, v132
	v_add_f32_e32 v124, v124, v125
	v_add_f32_e32 v123, v123, v124
	s_waitcnt vmcnt(0)
	v_lshlrev_b32_e32 v124, 16, v4
	v_and_b32_e32 v125, 0xffff0000, v4
	v_lshlrev_b32_e32 v126, 16, v5
	v_and_b32_e32 v127, 0xffff0000, v5
	v_pk_add_f32 v[128:129], v[42:43], v[126:127]
	v_pk_add_f32 v[130:131], v[40:41], v[124:125]
	v_mul_f32_e32 v125, v129, v129
	v_mul_f32_e32 v124, v131, v131
	v_fmac_f32_e32 v124, v130, v130
	v_fmac_f32_e32 v125, v128, v128
	v_add_f32_e32 v124, v124, v125
	v_add_f32_e32 v123, v123, v124
	v_lshlrev_b32_e32 v126, 16, v6
	v_and_b32_e32 v127, 0xffff0000, v6
	v_lshlrev_b32_e32 v124, 16, v7
	v_and_b32_e32 v125, 0xffff0000, v7
	v_pk_add_f32 v[124:125], v[46:47], v[124:125]
	v_pk_add_f32 v[126:127], v[44:45], v[126:127]
	v_mul_f32_e32 v195, v125, v125
	v_mul_f32_e32 v194, v127, v127
	v_fmac_f32_e32 v194, v126, v126
	v_fmac_f32_e32 v195, v124, v124
	v_add_f32_e32 v194, v194, v195
	v_add_f32_e32 v123, v123, v194
	v_mov_b32_e32 v195, v123
	v_cmp_gt_u32_e32 vcc, 16, v85
	s_and_b32 s51, s84, 0x80
	s_nop 1
	v_permlane16_swap_b32_e32 v123, v195
	v_add_f32_e32 v123, v123, v195
	v_mov_b32_e32 v195, v123
	s_nop 1
	v_permlane32_swap_b32_e32 v123, v195
	s_waitcnt lgkmcnt(0)
	v_add_f32_e32 v123, v123, v195
	s_and_saveexec_b64 s[56:57], vcc
	s_add_i32 s53, s51, s25
	v_or_b32_e32 v85, s53, v121
	v_lshl_add_u32 v85, v85, 2, s24
	ds_write_b32 v85, v123
	s_or_b64 exec, exec, s[56:57]
	s_add_i32 s51, s51, s82
	v_or_b32_e32 v85, s51, v121
	s_waitcnt lgkmcnt(0)
	s_barrier
	v_lshl_add_u32 v85, v85, 2, s24
	ds_read_b32 v85, v85
	v_lshlrev_b32_e32 v212, 16, v62
	v_and_b32_e32 v213, 0xffff0000, v62
	v_lshlrev_b32_e32 v214, 16, v63
	v_and_b32_e32 v215, 0xffff0000, v63
	s_waitcnt lgkmcnt(0)
	v_add_f32_e32 v85, v123, v85
	v_fmamk_f32 v85, v85, 0x3c000000, v200
	v_rsq_f32_e32 v194, v85
	v_ashrrev_i32_e32 v123, 31, v122
	v_lshlrev_b64 v[122:123], 11, v[122:123]
	v_ashrrev_i32_e32 v121, 31, v120
	v_pk_mul_f32 v[136:137], v[136:137], v[194:195] op_sel_hi:[1,0]
	v_pk_mul_f32 v[138:139], v[138:139], v[194:195] op_sel_hi:[1,0]
	v_pk_mul_f32 v[136:137], v[136:137], v[214:215]
	v_pk_mul_f32 v[138:139], v[138:139], v[212:213]
	v_lshl_add_u64 v[122:123], s[46:47], 0, v[122:123]
	v_cvt_pk_bf16_f32 v138, v138, v139
	v_cvt_pk_bf16_f32 v139, v136, v137
	v_lshl_add_u64 v[136:137], s[0:1], 1, v[122:123]
	v_lshlrev_b64 v[120:121], 1, v[120:121]
	v_lshl_add_u64 v[136:137], v[136:137], 0, v[120:121]
	global_store_dwordx2 v[136:137], v[138:139], off
	v_pk_mul_f32 v[134:135], v[134:135], v[194:195] op_sel_hi:[1,0]
	v_lshlrev_b32_e32 v138, 16, v60
	v_and_b32_e32 v139, 0xffff0000, v60
	v_pk_mul_f32 v[132:133], v[132:133], v[194:195] op_sel_hi:[1,0]
	v_lshlrev_b32_e32 v212, 16, v61
	v_and_b32_e32 v213, 0xffff0000, v61
	v_pk_mul_f32 v[134:135], v[134:135], v[138:139]
	v_pk_mul_f32 v[132:133], v[132:133], v[212:213]
	v_cvt_pk_bf16_f32 v134, v134, v135
	v_pk_mul_f32 v[128:129], v[128:129], v[194:195] op_sel_hi:[1,0]
	v_cvt_pk_bf16_f32 v135, v132, v133
	global_store_dwordx2 v[136:137], v[134:135], off offset:32
	v_pk_mul_f32 v[130:131], v[130:131], v[194:195] op_sel_hi:[1,0]
	v_lshlrev_b32_e32 v132, 16, v58
	v_and_b32_e32 v133, 0xffff0000, v58
	v_lshlrev_b32_e32 v134, 16, v59
	v_and_b32_e32 v135, 0xffff0000, v59
	v_pk_mul_f32 v[128:129], v[128:129], v[134:135]
	v_pk_mul_f32 v[130:131], v[130:131], v[132:133]
	v_pk_mul_f32 v[126:127], v[126:127], v[194:195] op_sel_hi:[1,0]
	v_cvt_pk_bf16_f32 v130, v130, v131
	v_cvt_pk_bf16_f32 v131, v128, v129
	v_lshlrev_b32_e32 v128, 16, v56
	v_and_b32_e32 v129, 0xffff0000, v56
	v_lshl_add_u64 v[122:123], s[22:23], 1, v[122:123]
	global_store_dwordx2 v[136:137], v[130:131], off offset:64
	v_pk_mul_f32 v[124:125], v[124:125], v[194:195] op_sel_hi:[1,0]
	v_lshlrev_b32_e32 v130, 16, v57
	v_and_b32_e32 v131, 0xffff0000, v57
	v_pk_mul_f32 v[126:127], v[126:127], v[128:129]
	v_lshl_add_u64 v[120:121], v[122:123], 0, v[120:121]
	s_mov_b64 s[56:57], 0
	v_pk_mul_f32 v[124:125], v[124:125], v[130:131]
	v_cvt_pk_bf16_f32 v126, v126, v127
	s_nop 0
	v_cvt_pk_bf16_f32 v127, v124, v125
	global_store_dwordx2 v[120:121], v[126:127], off

.LBB0_742:
	v_add_u32_e32 v8, s91, v8
	v_cvt_pk_bf16_f32 v20, v13, v10
	v_lshlrev_b32_e32 v10, 4, v8
	v_and_b32_e32 v10, 0xfffffc00, v10
	v_bitop3_b32 v8, v8, v9, 56 bitop3:0x6c
	v_add3_u32 v8, v11, v10, v8
	v_cvt_pk_bf16_f32 v21, v14, v15
	ds_write_b64 v8, v[20:21]
	s_waitcnt lgkmcnt(0)
	s_barrier
	v_add_u32_e32 v8, s27, v12
	v_add_u32_e32 v12, s33, v12
	v_add_u32_e32 v125, s97, v18
	ds_read_b128 v[8:11], v8
	ds_read_b128 v[12:15], v12
	ds_read_b128 v[20:23], v17
	ds_read_b128 v[24:27], v125
	ds_read_b128 v[28:31], v125 offset:4096
	ds_read_b128 v[32:35], v125 offset:8192
	ds_read_b128 v[36:39], v125 offset:12288
	ds_read_b128 v[40:43], v17 offset:1024
	ds_read_b128 v[44:47], v125 offset:1024
	ds_read_b128 v[48:51], v125 offset:5120
	ds_read_b128 v[52:55], v125 offset:9216
	ds_read_b128 v[56:59], v125 offset:13312
	v_add_u32_e32 v127, s3, v18
	v_add_u32_e32 v144, s62, v18
	v_add_u32_e32 v145, s61, v18
	ds_read_b128 v[60:63], v17 offset:2048
	ds_read_b128 v[128:131], v125 offset:2048
	ds_read_b128 v[132:135], v125 offset:6144
	ds_read_b128 v[136:139], v125 offset:10240
	ds_read_b128 v[140:143], v125 offset:14336
	s_waitcnt lgkmcnt(13)
	v_mfma_f32_16x16x32_bf16 v[24:27], v[24:27], v[20:23], 0
	s_waitcnt lgkmcnt(12)
	v_mfma_f32_16x16x32_bf16 v[28:31], v[28:31], v[20:23], 0
	s_waitcnt lgkmcnt(11)
	v_mfma_f32_16x16x32_bf16 v[32:35], v[32:35], v[20:23], 0
	s_waitcnt lgkmcnt(10)
	v_mfma_f32_16x16x32_bf16 v[18:21], v[36:39], v[20:23], 0
	s_waitcnt lgkmcnt(8)
	v_mfma_f32_16x16x32_bf16 v[22:25], v[44:47], v[40:43], v[24:27]
	ds_read_b128 v[36:39], v17 offset:3072
	s_waitcnt lgkmcnt(8)
	v_mfma_f32_16x16x32_bf16 v[26:29], v[48:51], v[40:43], v[28:31]
	s_waitcnt lgkmcnt(7)
	v_mfma_f32_16x16x32_bf16 v[30:33], v[52:55], v[40:43], v[32:35]
	ds_read_b128 v[44:47], v125 offset:3072
	ds_read_b128 v[48:51], v125 offset:7168
	ds_read_b128 v[52:55], v125 offset:11264
	ds_read_b128 v[192:195], v125 offset:15360
	s_waitcnt lgkmcnt(10)
	v_mfma_f32_16x16x32_bf16 v[18:21], v[56:59], v[40:43], v[18:21]
	s_waitcnt lgkmcnt(8)
	v_mfma_f32_16x16x32_bf16 v[22:25], v[128:131], v[60:63], v[22:25]
	ds_read_b128 v[40:43], v127
	ds_read_b128 v[56:59], v145 offset:49152
	s_waitcnt lgkmcnt(9)
	v_mfma_f32_16x16x32_bf16 v[26:29], v[132:135], v[60:63], v[26:29]
	s_waitcnt lgkmcnt(8)
	v_mfma_f32_16x16x32_bf16 v[30:33], v[136:139], v[60:63], v[30:33]
	ds_read_b128 v[128:131], v145 offset:51200
	ds_read_b128 v[132:135], v145 offset:53248
	ds_read_b128 v[136:139], v145 offset:55296
	s_waitcnt lgkmcnt(10)
	v_mfma_f32_16x16x32_bf16 v[18:21], v[140:143], v[60:63], v[18:21]
	s_waitcnt lgkmcnt(8)
	v_mfma_f32_16x16x32_bf16 v[22:25], v[44:47], v[36:39], v[22:25]
	s_waitcnt lgkmcnt(7)
	v_mfma_f32_16x16x32_bf16 v[26:29], v[48:51], v[36:39], v[26:29]
	ds_read_b128 v[44:47], v127 offset:1024
	ds_read_b128 v[48:51], v145 offset:50176
	s_waitcnt lgkmcnt(8)
	v_mfma_f32_16x16x32_bf16 v[30:33], v[52:55], v[36:39], v[30:33]
	ds_read_b128 v[52:55], v145 offset:52224
	ds_read_b128 v[140:143], v145 offset:54272
	ds_read_b128 v[212:215], v145 offset:56320
	s_waitcnt lgkmcnt(10)
	v_mfma_f32_16x16x32_bf16 v[18:21], v[192:195], v[36:39], v[18:21]
	s_waitcnt lgkmcnt(7)
	v_mfma_f32_16x16x32_bf16 v[26:29], v[128:131], v[40:43], v[26:29]
	ds_read_b128 v[128:131], v144 offset:32768
	ds_read_b128 v[192:195], v144 offset:33792
	s_waitcnt lgkmcnt(8)
	v_mfma_f32_16x16x32_bf16 v[30:33], v[132:135], v[40:43], v[30:33]
	ds_read_b128 v[34:37], v16 offset:49152
	ds_read_b128 v[132:135], v16 offset:50176
	ds_read_b128 v[216:219], v16 offset:51200
	ds_read_b128 v[220:223], v16 offset:52224
	v_mfma_f32_16x16x32_bf16 v[22:25], v[56:59], v[40:43], v[22:25]
	s_waitcnt lgkmcnt(11)
	v_mfma_f32_16x16x32_bf16 v[18:21], v[136:139], v[40:43], v[18:21]
	s_waitcnt lgkmcnt(9)
	v_mfma_f32_16x16x32_bf16 v[60:63], v[48:51], v[44:47], v[22:25]
	s_waitcnt lgkmcnt(8)
	v_mfma_f32_16x16x32_bf16 v[56:59], v[52:55], v[44:47], v[26:29]
	s_waitcnt lgkmcnt(7)
	v_mfma_f32_16x16x32_bf16 v[48:51], v[140:143], v[44:47], v[30:33]
	ds_read_b128 v[22:25], v16 offset:53248
	ds_read_b128 v[26:29], v16 offset:54272
	ds_read_b128 v[136:139], v16 offset:55296
	ds_read_b128 v[140:143], v16 offset:56320
	s_waitcnt lgkmcnt(10)
	v_mfma_f32_16x16x32_bf16 v[52:55], v[212:215], v[44:47], v[18:21]
	s_waitcnt lgkmcnt(7)
	v_mfma_f32_16x16x32_bf16 v[18:21], v[128:131], v[34:37], 0
	s_waitcnt lgkmcnt(6)
	v_mfma_f32_16x16x32_bf16 v[44:47], v[192:195], v[132:135], v[18:21]
	s_waitcnt lgkmcnt(5)
	v_mfma_f32_16x16x32_bf16 v[18:21], v[128:131], v[216:219], 0
	s_waitcnt lgkmcnt(4)
	v_mfma_f32_16x16x32_bf16 v[40:43], v[192:195], v[220:223], v[18:21]
	s_waitcnt lgkmcnt(3)
	v_mfma_f32_16x16x32_bf16 v[18:21], v[128:131], v[22:25], 0
	s_waitcnt lgkmcnt(2)
	v_mfma_f32_16x16x32_bf16 v[32:35], v[192:195], v[26:29], v[18:21]
	s_nop 5
	ds_read_b128 v[18:21], v16 offset:57344
	ds_read_b128 v[22:25], v16 offset:58368
	ds_read_b128 v[132:135], v16 offset:59392
	ds_read_b128 v[212:215], v16 offset:60416
	s_waitcnt lgkmcnt(5)
	v_mfma_f32_16x16x32_bf16 v[26:29], v[128:131], v[136:139], 0
	ds_read_b128 v[136:139], v16 offset:61440
	ds_read_b128 v[216:219], v16 offset:62464
	ds_read_b128 v[220:223], v16 offset:63488
	ds_read_b128 v[224:227], v16 offset:64512
	s_waitcnt lgkmcnt(8)
	v_mfma_f32_16x16x32_bf16 v[36:39], v[192:195], v[140:143], v[26:29]
	s_waitcnt lgkmcnt(7)
	v_mfma_f32_16x16x32_bf16 v[16:19], v[128:131], v[18:21], 0
	s_mov_b64 s[58:59], -1
	s_andn2_b64 vcc, exec, s[56:57]
	s_waitcnt lgkmcnt(6)
	v_mfma_f32_16x16x32_bf16 v[28:31], v[192:195], v[22:25], v[16:19]
	s_waitcnt lgkmcnt(5)
	v_mfma_f32_16x16x32_bf16 v[16:19], v[128:131], v[132:135], 0
	s_waitcnt lgkmcnt(4)
	v_mfma_f32_16x16x32_bf16 v[24:27], v[192:195], v[212:215], v[16:19]
	s_waitcnt lgkmcnt(3)
	v_mfma_f32_16x16x32_bf16 v[16:19], v[128:131], v[136:139], 0
	s_waitcnt lgkmcnt(2)
	v_mfma_f32_16x16x32_bf16 v[20:23], v[192:195], v[216:219], v[16:19]
	s_waitcnt lgkmcnt(1)
	v_mfma_f32_16x16x32_bf16 v[16:19], v[128:131], v[220:223], 0
	s_waitcnt lgkmcnt(0)
	v_mfma_f32_16x16x32_bf16 v[16:19], v[192:195], v[224:227], v[16:19]
	s_cbranch_vccnz .LBB0_746
	s_waitcnt vmcnt(1)
	v_lshlrev_b32_e32 v128, 16, v0
	v_and_b32_e32 v129, 0xffff0000, v0
	v_lshlrev_b32_e32 v130, 16, v1
	v_and_b32_e32 v131, 0xffff0000, v1
	v_pk_add_f32 v[142:143], v[62:63], v[130:131]
	v_pk_add_f32 v[144:145], v[60:61], v[128:129]
	v_mul_f32_e32 v127, v143, v143
	v_mul_f32_e32 v125, v145, v145
	v_lshlrev_b32_e32 v128, 16, v2
	v_and_b32_e32 v129, 0xffff0000, v2
	v_lshlrev_b32_e32 v130, 16, v3
	v_and_b32_e32 v131, 0xffff0000, v3
	v_fmac_f32_e32 v125, v144, v144
	v_fmac_f32_e32 v127, v142, v142
	v_pk_add_f32 v[136:137], v[58:59], v[130:131]
	v_pk_add_f32 v[138:139], v[56:57], v[128:129]
	v_add_f32_e32 v125, v125, v127
	v_mul_f32_e32 v127, v139, v139
	v_mul_f32_e32 v128, v137, v137
	v_fmac_f32_e32 v127, v138, v138
	v_fmac_f32_e32 v128, v136, v136
	v_add_f32_e32 v127, v127, v128
	s_waitcnt vmcnt(0)
	v_lshlrev_b32_e32 v128, 16, v4
	v_and_b32_e32 v129, 0xffff0000, v4
	v_lshlrev_b32_e32 v130, 16, v5
	v_and_b32_e32 v131, 0xffff0000, v5
	v_pk_add_f32 v[132:133], v[50:51], v[130:131]
	v_pk_add_f32 v[134:135], v[48:49], v[128:129]
	v_add_f32_e32 v125, v125, v127
	v_mul_f32_e32 v127, v135, v135
	v_mul_f32_e32 v128, v133, v133
	v_fmac_f32_e32 v127, v134, v134
	v_fmac_f32_e32 v128, v132, v132
	v_add_f32_e32 v127, v127, v128
	v_lshlrev_b32_e32 v130, 16, v6
	v_and_b32_e32 v131, 0xffff0000, v6
	v_lshlrev_b32_e32 v128, 16, v7
	v_and_b32_e32 v129, 0xffff0000, v7
	v_pk_add_f32 v[128:129], v[54:55], v[128:129]
	v_pk_add_f32 v[130:131], v[52:53], v[130:131]
	v_add_f32_e32 v125, v125, v127
	v_mul_f32_e32 v127, v131, v131
	v_mul_f32_e32 v140, v129, v129
	v_fmac_f32_e32 v127, v130, v130
	v_fmac_f32_e32 v140, v128, v128
	v_add_f32_e32 v127, v127, v140
	v_add_f32_e32 v125, v125, v127
	v_mov_b32_e32 v140, v125
	v_cmp_gt_u32_e32 vcc, 16, v190
	s_and_b32 s43, s83, 0x80
	s_nop 1
	v_permlane16_swap_b32_e32 v125, v140
	v_add_f32_e32 v125, v125, v140
	v_mov_b32_e32 v140, v125
	s_nop 1
	v_permlane32_swap_b32_e32 v125, v140
	s_waitcnt lgkmcnt(0)
	v_add_f32_e32 v125, v125, v140
	s_and_saveexec_b64 s[58:59], vcc
	s_add_i32 s49, s43, s25
	v_or_b32_e32 v127, s49, v64
	v_lshl_add_u32 v127, v127, 2, s24
	ds_write_b32 v127, v125
	s_or_b64 exec, exec, s[58:59]
	s_add_i32 s43, s43, s82
	v_or_b32_e32 v64, s43, v64
	s_waitcnt lgkmcnt(0)
	s_barrier
	v_lshl_add_u32 v64, v64, 2, s24
	ds_read_b32 v64, v64
	v_ashrrev_i32_e32 v127, 31, v126
	v_lshlrev_b64 v[126:127], 11, v[126:127]
	v_lshl_add_u64 v[126:127], s[46:47], 0, v[126:127]
	s_mov_b64 s[58:59], 0
	s_waitcnt lgkmcnt(0)
	v_add_f32_e32 v64, v125, v64
	v_ashrrev_i32_e32 v125, 31, v124
	v_lshlrev_b64 v[140:141], 2, v[124:125]
	v_lshl_add_u64 v[212:213], s[38:39], 0, v[140:141]
	global_load_dwordx4 v[192:195], v[212:213], off
	global_load_dwordx4 v[216:219], v[212:213], off offset:64
	global_load_dwordx4 v[220:223], v[212:213], off offset:128
	v_lshl_add_u64 v[224:225], s[40:41], 0, v[140:141]
	global_load_dwordx4 v[224:227], v[224:225], off
	v_fmamk_f32 v64, v64, 0x3c000000, v200
	v_rsq_f32_e32 v64, v64
	v_lshlrev_b64 v[124:125], 1, v[124:125]
	v_pk_mul_f32 v[142:143], v[142:143], v[64:65] op_sel_hi:[1,0]
	v_pk_mul_f32 v[144:145], v[144:145], v[64:65] op_sel_hi:[1,0]
	v_pk_mul_f32 v[138:139], v[138:139], v[64:65] op_sel_hi:[1,0]
	v_pk_mul_f32 v[136:137], v[136:137], v[64:65] op_sel_hi:[1,0]
	v_pk_mul_f32 v[132:133], v[132:133], v[64:65] op_sel_hi:[1,0]
	v_pk_mul_f32 v[134:135], v[134:135], v[64:65] op_sel_hi:[1,0]
	v_pk_mul_f32 v[130:131], v[130:131], v[64:65] op_sel_hi:[1,0]
	v_pk_mul_f32 v[128:129], v[128:129], v[64:65] op_sel_hi:[1,0]
	s_waitcnt vmcnt(3)
	v_pk_mul_f32 v[142:143], v[194:195], v[142:143]
	v_pk_mul_f32 v[144:145], v[192:193], v[144:145]
	v_lshlrev_b32_e32 v192, 16, v90
	v_and_b32_e32 v193, 0xffff0000, v90
	v_lshlrev_b32_e32 v194, 16, v91
	v_and_b32_e32 v195, 0xffff0000, v91
	v_pk_mul_f32 v[142:143], v[142:143], v[194:195]
	v_pk_mul_f32 v[144:145], v[144:145], v[192:193]
	s_nop 0
	v_cvt_pk_bf16_f32 v144, v144, v145
	v_cvt_pk_bf16_f32 v145, v142, v143
	v_lshl_add_u64 v[142:143], s[0:1], 1, v[126:127]
	v_lshl_add_u64 v[192:193], v[142:143], 0, v[124:125]
	global_store_dwordx2 v[192:193], v[144:145], off
	v_lshl_add_u64 v[126:127], s[22:23], 1, v[126:127]
	v_lshl_add_u64 v[124:125], v[126:127], 0, v[124:125]
	s_waitcnt vmcnt(3)
	v_pk_mul_f32 v[138:139], v[216:217], v[138:139]
	v_lshlrev_b32_e32 v142, 16, v88
	v_and_b32_e32 v143, 0xffff0000, v88
	v_pk_mul_f32 v[136:137], v[218:219], v[136:137]
	v_lshlrev_b32_e32 v144, 16, v89
	v_and_b32_e32 v145, 0xffff0000, v89
	v_pk_mul_f32 v[138:139], v[138:139], v[142:143]
	v_pk_mul_f32 v[136:137], v[136:137], v[144:145]
	v_cvt_pk_bf16_f32 v138, v138, v139
	s_nop 0
	v_cvt_pk_bf16_f32 v139, v136, v137
	global_store_dwordx2 v[192:193], v[138:139], off offset:32
	s_waitcnt vmcnt(3)
	v_pk_mul_f32 v[132:133], v[132:133], v[222:223]
	v_pk_mul_f32 v[134:135], v[134:135], v[220:221]
	v_lshlrev_b32_e32 v136, 16, v86
	v_and_b32_e32 v137, 0xffff0000, v86
	v_lshlrev_b32_e32 v138, 16, v87
	v_and_b32_e32 v139, 0xffff0000, v87
	v_pk_mul_f32 v[132:133], v[132:133], v[138:139]
	v_pk_mul_f32 v[134:135], v[134:135], v[136:137]
	s_nop 0
	v_cvt_pk_bf16_f32 v134, v134, v135
	v_cvt_pk_bf16_f32 v135, v132, v133
	global_store_dwordx2 v[192:193], v[134:135], off offset:64
	s_waitcnt vmcnt(3)
	v_pk_mul_f32 v[130:131], v[130:131], v[224:225]
	v_lshlrev_b32_e32 v132, 16, v84
	v_and_b32_e32 v133, 0xffff0000, v84
	v_pk_mul_f32 v[128:129], v[128:129], v[226:227]
	v_lshlrev_b32_e32 v134, 16, v85
	v_and_b32_e32 v135, 0xffff0000, v85
	v_pk_mul_f32 v[130:131], v[130:131], v[132:133]
	v_pk_mul_f32 v[128:129], v[128:129], v[134:135]
	v_cvt_pk_bf16_f32 v130, v130, v131
	s_nop 0
	v_cvt_pk_bf16_f32 v131, v128, v129
	global_store_dwordx2 v[124:125], v[130:131], off
